# row-pass wave sums: xor-1/2/4/8 butterfly steps through DPP instead of ds_swizzle round trips (bit-identical), plus s_nop padding at cold spots that moves the MoE GEMM loops by 16 bytes and keeps the
# speedup vs baseline: 1.0025x; 1.0025x over previous
; #define RP_UNPK(V_, H_) ((H_) ? (f32x4){bflo((V_)[2]), bfhi((V_)[2]), bflo((V_)[3]), bfhi((V_)[3])} : (f32x4){bflo((V_)[0]), bfhi((V_)[0]), bflo((V_)[1]), bfhi((V_)[1])})
; template <int MODE, bool FIRSTX>
; __device__ __forceinline__ void row_pass(Frame& F, int layer, bool final_out, int row0) {
;     ...
;         f32x4 v[4];
; #pragma unroll
;         for (int q = 0; q < 4; ++q) v[q] = FIRSTX ? xf[q] : RP_UNPK(xb[q >> 1], q & 1);
;         if (MODE != 0) {
; #pragma unroll
;             for (int q = 0; q < 4; ++q) { f32x4 y = (f32x4){0.f, 0.f, 0.f, 0.f};
; #pragma unroll
;                 for (int k = 0; k < NY; ++k) { if (MODE == 2) { const unsigned w8 = yb[k][q >> 1][q & 1]; const f32x2 lo = __builtin_amdgcn_cvt_pk_f32_fp8((int)w8, false), hi = __builtin_amdgcn_cvt_pk_f32_fp8((int)w8, true); y += (f32x4){lo.x, lo.y, hi.x, hi.y}; }
;                                                 else y += RP_UNPK(yb[k][q >> 1], q & 1); }
;                 if (MODE == 2) y = y * (1.0f / YK8_SCALE);
;                 v[q] = v[q] * DN_ALPHA + gt[q] * y; }
;             float s = 0.f;
; #pragma unroll
;             for (int q = 0; q < 4; ++q) s += (v[q][0] + v[q][1]) + (v[q][2] + v[q][3]);
;             const float mean = wave_sum(s) * (1.0f / DM); float qq = 0.f;
; #pragma unroll
;             for (int q = 0; q < 4; ++q) { v[q] = v[q] - mean; qq += (v[q][0] * v[q][0] + v[q][1] * v[q][1]) + (v[q][2] * v[q][2] + v[q][3] * v[q][3]); }
;             const float rstd = 1.0f / sqrtf(wave_sum(qq) * (1.0f / DM) + LN_EPS);
.Lrp1_common:
	v_lshlrev_b32_e32 v128, 16, v102
	v_and_b32_e32 v129, 0xffff0000, v102
	v_lshlrev_b32_e32 v102, 16, v103
	v_and_b32_e32 v103, 0xffff0000, v103
	v_pk_add_f32 v[102:103], v[102:103], 0 op_sel_hi:[1,0]
	v_pk_add_f32 v[128:129], v[128:129], 0 op_sel_hi:[1,0]
	v_lshlrev_b32_e32 v120, 16, v110
	v_and_b32_e32 v121, 0xffff0000, v110
	v_lshlrev_b32_e32 v110, 16, v111
	v_and_b32_e32 v111, 0xffff0000, v111
	v_pk_mul_f32 v[128:129], v[128:129], v[46:47]
	v_pk_mul_f32 v[102:103], v[102:103], v[48:49]
	v_lshlrev_b32_e32 v122, 16, v112
	v_pk_fma_f32 v[102:103], v[110:111], s[62:63], v[102:103] op_sel_hi:[1,0,1]
	v_pk_fma_f32 v[110:111], v[120:121], s[62:63], v[128:129] op_sel_hi:[1,0,1]
	v_lshlrev_b32_e32 v120, 16, v104
	v_and_b32_e32 v121, 0xffff0000, v104
	v_lshlrev_b32_e32 v104, 16, v105
	v_and_b32_e32 v105, 0xffff0000, v105
	v_pk_add_f32 v[104:105], v[104:105], 0 op_sel_hi:[1,0]
	v_pk_add_f32 v[120:121], v[120:121], 0 op_sel_hi:[1,0]
	v_and_b32_e32 v123, 0xffff0000, v112
	v_lshlrev_b32_e32 v112, 16, v113
	v_and_b32_e32 v113, 0xffff0000, v113
	v_pk_mul_f32 v[120:121], v[120:121], v[42:43]
	v_pk_mul_f32 v[104:105], v[104:105], v[44:45]
	v_lshlrev_b32_e32 v124, 16, v106
	v_pk_fma_f32 v[104:105], v[112:113], s[62:63], v[104:105] op_sel_hi:[1,0,1]
	v_pk_fma_f32 v[112:113], v[122:123], s[62:63], v[120:121] op_sel_hi:[1,0,1]
	v_lshlrev_b32_e32 v120, 16, v98
	v_and_b32_e32 v121, 0xffff0000, v98
	v_lshlrev_b32_e32 v98, 16, v99
	v_and_b32_e32 v99, 0xffff0000, v99
	v_pk_add_f32 v[98:99], v[98:99], 0 op_sel_hi:[1,0]
	v_pk_add_f32 v[120:121], v[120:121], 0 op_sel_hi:[1,0]
	v_and_b32_e32 v125, 0xffff0000, v106
	v_lshlrev_b32_e32 v106, 16, v107
	v_and_b32_e32 v107, 0xffff0000, v107
	v_pk_mul_f32 v[120:121], v[120:121], v[78:79]
	v_pk_mul_f32 v[98:99], v[98:99], v[80:81]
	v_lshlrev_b32_e32 v126, 16, v108
	v_pk_fma_f32 v[98:99], v[106:107], s[62:63], v[98:99] op_sel_hi:[1,0,1]
	v_pk_fma_f32 v[106:107], v[124:125], s[62:63], v[120:121] op_sel_hi:[1,0,1]
	v_lshlrev_b32_e32 v120, 16, v100
	v_and_b32_e32 v121, 0xffff0000, v100
	v_lshlrev_b32_e32 v100, 16, v101
	v_and_b32_e32 v101, 0xffff0000, v101
	v_pk_add_f32 v[100:101], v[100:101], 0 op_sel_hi:[1,0]
	v_pk_add_f32 v[120:121], v[120:121], 0 op_sel_hi:[1,0]
	v_and_b32_e32 v127, 0xffff0000, v108
	v_lshlrev_b32_e32 v108, 16, v109
	v_and_b32_e32 v109, 0xffff0000, v109
	v_pk_mul_f32 v[120:121], v[120:121], v[70:71]
	v_pk_mul_f32 v[100:101], v[100:101], v[72:73]
	v_add_f32_e32 v122, v104, v105
	v_pk_fma_f32 v[100:101], v[108:109], s[62:63], v[100:101] op_sel_hi:[1,0,1]
	v_pk_fma_f32 v[108:109], v[126:127], s[62:63], v[120:121] op_sel_hi:[1,0,1]
	v_add_f32_e32 v120, v110, v111
	v_add_f32_e32 v121, v102, v103
	v_add_f32_e32 v120, v120, v121
	v_add_f32_e32 v121, v112, v113
	v_add_f32_e32 v120, 0, v120
	v_add_f32_e32 v121, v121, v122
	v_add_f32_e32 v120, v121, v120
	v_add_f32_e32 v121, v106, v107
	v_add_f32_e32 v122, v98, v99
	v_add_f32_e32 v121, v121, v122
	v_add_f32_e32 v120, v121, v120
	v_add_f32_e32 v121, v108, v109
	v_add_f32_e32 v122, v100, v101
	v_add_f32_e32 v121, v121, v122
	v_add_f32_e32 v120, v121, v120
	s_nop 1
	v_add_f32_dpp v120, v120, v120 quad_perm:[1,0,3,2] row_mask:0xf bank_mask:0xf
	s_add_i32 s11, s11, 1
	v_lshl_add_u64 v[118:119], v[118:119], 0, s[50:51]
	s_cmp_lt_i32 s1, s14
	s_nop 1
	v_add_f32_dpp v120, v120, v120 quad_perm:[2,3,0,1] row_mask:0xf bank_mask:0xf
	s_nop 1
	v_add_f32_dpp v120, v120, v120 row_half_mirror row_mask:0xf bank_mask:0xf
	s_nop 1
	v_add_f32_dpp v120, v120, v120 row_mirror row_mask:0xf bank_mask:0xf
	s_waitcnt lgkmcnt(0)
	ds_swizzle_b32 v121, v120 offset:swizzle(SWAP,16)
	s_waitcnt lgkmcnt(0)
	v_add_f32_e32 v120, v120, v121
	v_mov_b32_e32 v121, v120
	s_nop 1
	v_permlane32_swap_b32_e32 v120, v121
	v_add_f32_e32 v120, v120, v121
	v_fmac_f32_e32 v103, 0xba800000, v120
	v_fmac_f32_e32 v111, 0xba800000, v120
	v_fmamk_f32 v102, v120, 0xba800000, v102
	v_fmamk_f32 v110, v120, 0xba800000, v110
	v_mul_f32_e32 v121, v111, v111
	v_mul_f32_e32 v122, v103, v103
	v_fmac_f32_e32 v121, v110, v110
	v_fmac_f32_e32 v122, v102, v102
	v_fmac_f32_e32 v105, 0xba800000, v120
	v_fmac_f32_e32 v113, 0xba800000, v120
	v_add_f32_e32 v121, v121, v122
	v_fmamk_f32 v104, v120, 0xba800000, v104
	v_fmamk_f32 v112, v120, 0xba800000, v112
	v_mul_f32_e32 v122, v113, v113
	v_mul_f32_e32 v123, v105, v105
	v_fmac_f32_e32 v122, v112, v112
	v_fmac_f32_e32 v123, v104, v104
	v_add_f32_e32 v122, v122, v123
	v_fmac_f32_e32 v99, 0xba800000, v120
	v_fmac_f32_e32 v107, 0xba800000, v120
	v_add_f32_e32 v121, v121, v122
	v_fmamk_f32 v98, v120, 0xba800000, v98
	v_fmamk_f32 v106, v120, 0xba800000, v106
	v_mul_f32_e32 v122, v107, v107
	v_mul_f32_e32 v123, v99, v99
	v_fmac_f32_e32 v122, v106, v106
	v_fmac_f32_e32 v123, v98, v98
	v_add_f32_e32 v122, v122, v123
	v_fmac_f32_e32 v101, 0xba800000, v120
	v_fmac_f32_e32 v109, 0xba800000, v120
	v_add_f32_e32 v121, v122, v121
	v_fmamk_f32 v100, v120, 0xba800000, v100
	v_fmamk_f32 v108, v120, 0xba800000, v108
	v_mul_f32_e32 v120, v109, v109
	v_mul_f32_e32 v122, v101, v101
	v_fmac_f32_e32 v120, v108, v108
	v_fmac_f32_e32 v122, v100, v100
	v_add_f32_e32 v120, v120, v122
	v_add_f32_e32 v120, v120, v121
	s_nop 1
	v_add_f32_dpp v120, v120, v120 quad_perm:[1,0,3,2] row_mask:0xf bank_mask:0xf
	s_nop 1
	v_add_f32_dpp v120, v120, v120 quad_perm:[2,3,0,1] row_mask:0xf bank_mask:0xf
	s_nop 1
	v_add_f32_dpp v120, v120, v120 row_half_mirror row_mask:0xf bank_mask:0xf
	s_nop 1
	v_add_f32_dpp v120, v120, v120 row_mirror row_mask:0xf bank_mask:0xf
	s_waitcnt lgkmcnt(0)
	ds_swizzle_b32 v121, v120 offset:swizzle(SWAP,16)
	s_waitcnt lgkmcnt(0)
; __device__ __forceinline__ unsigned pk2(float lo, float hi) { return f2bf(lo) | (f2bf(hi) << 16); }
; __device__ __forceinline__ unsigned cvt_fp8x4(float a, float b, float c, float d) { int w = __builtin_amdgcn_cvt_pk_fp8_f32(a, b, 0, false); w = __builtin_amdgcn_cvt_pk_fp8_f32(c, d, w, true); return (unsigned)w; }
; template <int MODE, bool FIRSTX>
; __device__ __forceinline__ void row_pass(Frame& F, int layer, bool final_out, int row0) {
;     ...
;             const float rstd = 1.0f / sqrtf(wave_sum(qq) * (1.0f / DM) + LN_EPS);
; #pragma unroll
;             for (int q = 0; q < 4; ++q) v[q] = v[q] * rstd * lg[q] + lb[q];
;             if (final_out) { if (row >= NCTX) {
; #pragma unroll
;                 for (int q = 0; q < 4; ++q) *(f32x4*)(F.out + (size_t)(row - NCTX) * DM + RP_COL(q)) = v[q]; } }
;             else {
; #pragma unroll
;                 for (int j = 0; j < 2; ++j) { u32x4 w; w.x = pk2(v[2 * j][0], v[2 * j][1]); w.y = pk2(v[2 * j][2], v[2 * j][3]); w.z = pk2(v[2 * j + 1][0], v[2 * j + 1][1]); w.w = pk2(v[2 * j + 1][2], v[2 * j + 1][3]);
;                     *(u32x4*)(X + (size_t)row * DM + lc + 512 * j) = w; } }
;         }
;         if (!final_out) {
; #pragma unroll
;             for (int j = 0; j < 2; ++j) { const f32x4 h0 = v[2 * j] * (sc[2 * j] + 1.0f) + sh[2 * j], h1 = v[2 * j + 1] * (sc[2 * j + 1] + 1.0f) + sh[2 * j + 1];
;                 if (MODE == 1 || (nlayer % 3) == 2) { u32x4 w; w.x = pk2(h0[0], h0[1]); w.y = pk2(h0[2], h0[3]); w.z = pk2(h1[0], h1[1]); w.w = pk2(h1[2], h1[3]);
;                     *(u32x4*)(H + (size_t)row * DM + lc + 512 * j) = w; }
;                 if (MODE == 1 || (nlayer % 3) != 2) {                                u32x2 w8; w8.x = cvt_fp8x4(h0[0], h0[1], h0[2], h0[3]); w8.y = cvt_fp8x4(h1[0], h1[1], h1[2], h1[3]); *(u32x2*)(F.ws + WS_H8 + (size_t)row * DM + lc + 512 * j) = w8; } }
	v_add_f32_e32 v120, v120, v121
	v_mov_b32_e32 v121, v120
	s_nop 1
	v_permlane32_swap_b32_e32 v120, v121
	v_add_f32_e32 v120, v120, v121
	v_fmamk_f32 v120, v120, 0x3a800000, v188
	v_mul_f32_e32 v121, 0x4f800000, v120
	v_cmp_gt_f32_e32 vcc, s31, v120
	s_nop 1
	v_cndmask_b32_e32 v120, v120, v121, vcc
	v_sqrt_f32_e32 v121, v120
	s_nop 0
	v_add_u32_e32 v122, -1, v121
	v_fma_f32 v123, -v122, v121, v120
	v_cmp_ge_f32_e64 s[2:3], 0, v123
	v_add_u32_e32 v123, 1, v121
	s_nop 0
	v_cndmask_b32_e64 v122, v121, v122, s[2:3]
	v_fma_f32 v121, -v123, v121, v120
	v_cmp_lt_f32_e64 s[2:3], 0, v121
	s_nop 1
	v_cndmask_b32_e64 v121, v122, v123, s[2:3]
	v_mul_f32_e32 v122, 0x37800000, v121
	v_cndmask_b32_e32 v121, v121, v122, vcc
	v_cmp_class_f32_e32 vcc, v120, v189
	s_nop 1
	v_cndmask_b32_e32 v120, v121, v120, vcc
	v_div_scale_f32 v121, s[2:3], v120, v120, 1.0
	v_rcp_f32_e32 v122, v121
	s_nop 0
	v_fma_f32 v123, -v121, v122, 1.0
	v_fmac_f32_e32 v122, v123, v122
	v_div_scale_f32 v123, vcc, 1.0, v120, 1.0
	v_mul_f32_e32 v124, v123, v122
	v_fma_f32 v125, -v121, v124, v123
	v_fmac_f32_e32 v124, v125, v122
	v_fma_f32 v121, -v121, v124, v123
	v_div_fmas_f32 v121, v121, v122, v124
	v_div_fixup_f32 v120, v121, v120, 1.0
	v_pk_mul_f32 v[110:111], v[110:111], v[120:121] op_sel_hi:[1,0]
	v_pk_mul_f32 v[98:99], v[98:99], v[120:121] op_sel_hi:[1,0]
	v_pk_fma_f32 v[110:111], v[2:3], v[110:111], v[6:7]
	v_pk_fma_f32 v[122:123], v[20:21], v[98:99], v[24:25]
	v_pk_mul_f32 v[98:99], v[100:101], v[120:121] op_sel_hi:[1,0]
	v_pk_mul_f32 v[102:103], v[102:103], v[120:121] op_sel_hi:[1,0]
	v_pk_mul_f32 v[112:113], v[112:113], v[120:121] op_sel_hi:[1,0]
	v_pk_mul_f32 v[104:105], v[104:105], v[120:121] op_sel_hi:[1,0]
	v_pk_mul_f32 v[106:107], v[106:107], v[120:121] op_sel_hi:[1,0]
	v_pk_mul_f32 v[100:101], v[108:109], v[120:121] op_sel_hi:[1,0]
	v_pk_fma_f32 v[120:121], v[28:29], v[98:99], v[32:33]
	v_bfe_u32 v98, v110, 16, 1
	v_add3_u32 v98, v110, v98, s43
	v_bfe_u32 v99, v111, 16, 1
	v_pk_fma_f32 v[102:103], v[4:5], v[102:103], v[8:9]
	v_lshrrev_b32_e32 v98, 16, v98
	v_add3_u32 v99, v111, v99, s43
	v_and_or_b32 v98, v99, s33, v98
	v_bfe_u32 v99, v102, 16, 1
	v_pk_fma_f32 v[108:109], v[26:27], v[100:101], v[30:31]
	v_add3_u32 v99, v102, v99, s43
	v_bfe_u32 v100, v103, 16, 1
	v_pk_fma_f32 v[112:113], v[10:11], v[112:113], v[14:15]
	v_lshrrev_b32_e32 v99, 16, v99
	v_add3_u32 v100, v103, v100, s43
	v_and_or_b32 v99, v100, s33, v99
	v_bfe_u32 v100, v112, 16, 1
	v_add3_u32 v100, v112, v100, s43
	v_bfe_u32 v101, v113, 16, 1
	v_pk_fma_f32 v[104:105], v[12:13], v[104:105], v[16:17]
	v_lshrrev_b32_e32 v100, 16, v100
	v_add3_u32 v101, v113, v101, s43
	v_and_or_b32 v100, v101, s33, v100
	v_bfe_u32 v101, v104, 16, 1
	v_add3_u32 v101, v104, v101, s43
	v_bfe_u32 v126, v105, 16, 1
	v_lshl_add_u64 v[124:125], s[74:75], 0, v[114:115]
	v_lshrrev_b32_e32 v101, 16, v101
	v_add3_u32 v126, v105, v126, s43
	v_and_or_b32 v101, v126, s33, v101
	v_add_co_u32_e32 v126, vcc, s39, v124
	v_pk_fma_f32 v[106:107], v[18:19], v[106:107], v[22:23]
	s_nop 0
	v_addc_co_u32_e32 v127, vcc, 0, v125, vcc
	global_store_dwordx4 v[126:127], v[98:101], off
	v_bfe_u32 v128, v121, 16, 1
	v_add3_u32 v128, v121, v128, s43
	v_bfe_u32 v98, v106, 16, 1
	v_add3_u32 v98, v106, v98, s43
	v_bfe_u32 v99, v107, 16, 1
	v_lshrrev_b32_e32 v98, 16, v98
	v_add3_u32 v99, v107, v99, s43
	v_and_or_b32 v98, v99, s33, v98
	v_bfe_u32 v99, v122, 16, 1
	v_add3_u32 v99, v122, v99, s43
	v_bfe_u32 v100, v123, 16, 1
	v_lshrrev_b32_e32 v99, 16, v99
	v_add3_u32 v100, v123, v100, s43
	v_and_or_b32 v99, v100, s33, v99
	v_bfe_u32 v100, v108, 16, 1
	v_add3_u32 v100, v108, v100, s43
	v_bfe_u32 v101, v109, 16, 1
	v_lshrrev_b32_e32 v100, 16, v100
	v_add3_u32 v101, v109, v101, s43
	v_and_or_b32 v100, v101, s33, v100
	v_bfe_u32 v101, v120, 16, 1
	v_add3_u32 v101, v120, v101, s43
	v_lshrrev_b32_e32 v101, 16, v101
	v_and_or_b32 v101, v128, s33, v101
	global_store_dwordx4 v[126:127], v[98:101], off offset:1024
	v_lshl_add_u64 v[114:115], v[114:115], 0, s[50:51]
	s_nop 0
	v_pk_add_f32 v[98:99], v[76:77], 1.0 op_sel_hi:[1,0]
	v_pk_add_f32 v[100:101], v[74:75], 1.0 op_sel_hi:[1,0]
	v_pk_fma_f32 v[102:103], v[98:99], v[102:103], v[64:65]
	v_pk_fma_f32 v[110:111], v[100:101], v[110:111], v[62:63]
	v_pk_add_f32 v[98:99], v[68:69], 1.0 op_sel_hi:[1,0]
	v_pk_add_f32 v[100:101], v[66:67], 1.0 op_sel_hi:[1,0]
	v_pk_fma_f32 v[104:105], v[98:99], v[104:105], v[60:61]
	v_and_b32_sdwa v99, v110, v185 dst_sel:DWORD dst_unused:UNUSED_PAD src0_sel:WORD_1 src1_sel:DWORD
	v_pk_fma_f32 v[112:113], v[100:101], v[112:113], v[58:59]
	v_add3_u32 v100, v110, v99, s43
	v_and_b32_sdwa v99, v103, v185 dst_sel:DWORD dst_unused:UNUSED_PAD src0_sel:WORD_1 src1_sel:DWORD
	v_and_b32_sdwa v101, v111, v185 dst_sel:DWORD dst_unused:UNUSED_PAD src0_sel:WORD_1 src1_sel:DWORD
; __device__ __forceinline__ unsigned pk2(float lo, float hi) { return f2bf(lo) | (f2bf(hi) << 16); }
; __device__ __forceinline__ unsigned cvt_fp8x4(float a, float b, float c, float d) { int w = __builtin_amdgcn_cvt_pk_fp8_f32(a, b, 0, false); w = __builtin_amdgcn_cvt_pk_fp8_f32(c, d, w, true); return (unsigned)w; }
; template <int MODE, bool FIRSTX>
; __device__ __forceinline__ void row_pass(Frame& F, int layer, bool final_out, int row0) {
;     ...
;         if (!final_out) {
; #pragma unroll
;             for (int j = 0; j < 2; ++j) { const f32x4 h0 = v[2 * j] * (sc[2 * j] + 1.0f) + sh[2 * j], h1 = v[2 * j + 1] * (sc[2 * j + 1] + 1.0f) + sh[2 * j + 1];
;                 if (MODE == 1 || (nlayer % 3) == 2) { u32x4 w; w.x = pk2(h0[0], h0[1]); w.y = pk2(h0[2], h0[3]); w.z = pk2(h1[0], h1[1]); w.w = pk2(h1[2], h1[3]);
;                     *(u32x4*)(H + (size_t)row * DM + lc + 512 * j) = w; }
;                 if (MODE == 1 || (nlayer % 3) != 2) {                                u32x2 w8; w8.x = cvt_fp8x4(h0[0], h0[1], h0[2], h0[3]); w8.y = cvt_fp8x4(h1[0], h1[1], h1[2], h1[3]); *(u32x2*)(F.ws + WS_H8 + (size_t)row * DM + lc + 512 * j) = w8; } }
;         }
; #pragma unroll
;         for (int q = 0; q < 4; ++q) xf[q] = xfn[q];
; #pragma unroll
;         for (int j = 0; j < 2; ++j) { xb[j] = xbn[j];
; #pragma unroll
;             for (int k = 0; k < (NY ? NY : 1); ++k) yb[k][j] = ybn[k][j]; }
	v_and_b32_sdwa v98, v102, v185 dst_sel:DWORD dst_unused:UNUSED_PAD src0_sel:WORD_1 src1_sel:DWORD
	v_add3_u32 v99, v103, v99, s43
	v_add3_u32 v101, v111, v101, s43
	v_add3_u32 v98, v102, v98, s43
	v_and_b32_e32 v99, 0xffff0000, v99
	v_and_b32_e32 v101, 0xffff0000, v101
	v_or_b32_sdwa v99, v99, v98 dst_sel:DWORD dst_unused:UNUSED_PAD src0_sel:DWORD src1_sel:WORD_1
	v_or_b32_sdwa v98, v101, v100 dst_sel:DWORD dst_unused:UNUSED_PAD src0_sel:DWORD src1_sel:WORD_1
	v_and_b32_sdwa v101, v112, v185 dst_sel:DWORD dst_unused:UNUSED_PAD src0_sel:WORD_1 src1_sel:DWORD
	v_add3_u32 v126, v112, v101, s43
	v_and_b32_sdwa v101, v105, v185 dst_sel:DWORD dst_unused:UNUSED_PAD src0_sel:WORD_1 src1_sel:DWORD
	v_and_b32_sdwa v127, v113, v185 dst_sel:DWORD dst_unused:UNUSED_PAD src0_sel:WORD_1 src1_sel:DWORD
	v_and_b32_sdwa v100, v104, v185 dst_sel:DWORD dst_unused:UNUSED_PAD src0_sel:WORD_1 src1_sel:DWORD
	v_add3_u32 v101, v105, v101, s43
	v_add3_u32 v127, v113, v127, s43
	v_add3_u32 v100, v104, v100, s43
	v_and_b32_e32 v101, 0xffff0000, v101
	v_and_b32_e32 v127, 0xffff0000, v127
	v_or_b32_sdwa v101, v101, v100 dst_sel:DWORD dst_unused:UNUSED_PAD src0_sel:DWORD src1_sel:WORD_1
	v_or_b32_sdwa v100, v127, v126 dst_sel:DWORD dst_unused:UNUSED_PAD src0_sel:DWORD src1_sel:WORD_1
	v_mov_b32_e32 v126, v1
	v_cvt_pk_fp8_f32 v126, v110, v111
	v_mov_b32_e32 v127, v1
	v_add_co_u32_e32 v110, vcc, s28, v124
	v_cvt_pk_fp8_f32 v127, v112, v113
	s_nop 0
	v_addc_co_u32_e32 v111, vcc, 0, v125, vcc
	global_store_dwordx4 v[110:111], v[98:101], off
	v_cvt_pk_fp8_f32 v126, v102, v103 op_sel:[0,0,1]
	v_cvt_pk_fp8_f32 v127, v104, v105 op_sel:[0,0,1]
	v_lshl_add_u64 v[98:99], s[74:75], 0, v[116:117]
	v_add_co_u32_e32 v102, vcc, s38, v98
	v_pk_add_f32 v[100:101], v[94:95], 1.0 op_sel_hi:[1,0]
	s_nop 0
	v_addc_co_u32_e32 v103, vcc, 0, v99, vcc
	v_pk_add_f32 v[98:99], v[96:97], 1.0 op_sel_hi:[1,0]
	v_pk_fma_f32 v[100:101], v[100:101], v[106:107], v[86:87]
	v_pk_fma_f32 v[104:105], v[98:99], v[122:123], v[88:89]
	v_pk_add_f32 v[98:99], v[92:93], 1.0 op_sel_hi:[1,0]
	v_pk_add_f32 v[106:107], v[90:91], 1.0 op_sel_hi:[1,0]
	v_pk_fma_f32 v[112:113], v[98:99], v[120:121], v[84:85]
	v_and_b32_sdwa v99, v100, v185 dst_sel:DWORD dst_unused:UNUSED_PAD src0_sel:WORD_1 src1_sel:DWORD
	v_pk_fma_f32 v[106:107], v[106:107], v[108:109], v[82:83]
	v_add3_u32 v108, v100, v99, s43
	v_and_b32_sdwa v99, v105, v185 dst_sel:DWORD dst_unused:UNUSED_PAD src0_sel:WORD_1 src1_sel:DWORD
	v_and_b32_sdwa v109, v101, v185 dst_sel:DWORD dst_unused:UNUSED_PAD src0_sel:WORD_1 src1_sel:DWORD
	v_and_b32_sdwa v98, v104, v185 dst_sel:DWORD dst_unused:UNUSED_PAD src0_sel:WORD_1 src1_sel:DWORD
	v_add3_u32 v99, v105, v99, s43
	v_add3_u32 v109, v101, v109, s43
	v_add3_u32 v98, v104, v98, s43
	v_and_b32_e32 v99, 0xffff0000, v99
	v_and_b32_e32 v109, 0xffff0000, v109
	v_or_b32_sdwa v99, v99, v98 dst_sel:DWORD dst_unused:UNUSED_PAD src0_sel:DWORD src1_sel:WORD_1
	v_or_b32_sdwa v98, v109, v108 dst_sel:DWORD dst_unused:UNUSED_PAD src0_sel:DWORD src1_sel:WORD_1
	v_and_b32_sdwa v108, v112, v185 dst_sel:DWORD dst_unused:UNUSED_PAD src0_sel:WORD_1 src1_sel:DWORD
	v_and_b32_sdwa v109, v106, v185 dst_sel:DWORD dst_unused:UNUSED_PAD src0_sel:WORD_1 src1_sel:DWORD
	v_add3_u32 v120, v106, v109, s43
	v_add3_u32 v121, v112, v108, s43
	v_and_b32_sdwa v108, v113, v185 dst_sel:DWORD dst_unused:UNUSED_PAD src0_sel:WORD_1 src1_sel:DWORD
	v_and_b32_sdwa v109, v107, v185 dst_sel:DWORD dst_unused:UNUSED_PAD src0_sel:WORD_1 src1_sel:DWORD
	v_add3_u32 v122, v113, v108, s43
	v_add3_u32 v123, v107, v109, s43
	v_mov_b32_e32 v108, v1
	v_mov_b32_e32 v109, v1
	v_cvt_pk_fp8_f32 v108, v100, v101
	v_cvt_pk_fp8_f32 v109, v106, v107
	v_and_b32_e32 v100, 0xffff0000, v122
	v_and_b32_e32 v106, 0xffff0000, v123
	v_cvt_pk_fp8_f32 v108, v104, v105 op_sel:[0,0,1]
	v_cvt_pk_fp8_f32 v109, v112, v113 op_sel:[0,0,1]
	v_or_b32_sdwa v101, v100, v121 dst_sel:DWORD dst_unused:UNUSED_PAD src0_sel:DWORD src1_sel:WORD_1
	v_or_b32_sdwa v100, v106, v120 dst_sel:DWORD dst_unused:UNUSED_PAD src0_sel:DWORD src1_sel:WORD_1
	global_store_dwordx2 v[102:103], v[126:127], off
	global_store_dwordx4 v[110:111], v[98:101], off offset:1024
	global_store_dwordx2 v[102:103], v[108:109], off offset:512
	v_lshl_add_u64 v[116:117], v[116:117], 0, s[54:55]
	s_waitcnt vmcnt(6)
	v_mov_b32_e32 v102, v54
	v_mov_b32_e32 v103, v55
	v_mov_b32_e32 v104, v56
	v_mov_b32_e32 v105, v57
	v_mov_b32_e32 v98, v50
	v_mov_b32_e32 v99, v51
	v_mov_b32_e32 v100, v52
	v_mov_b32_e32 v101, v53
	v_mov_b32_e32 v110, v38
	v_mov_b32_e32 v111, v39
	v_mov_b32_e32 v112, v40
	v_mov_b32_e32 v113, v41
	v_mov_b32_e32 v106, v34
	v_mov_b32_e32 v107, v35
	v_mov_b32_e32 v108, v36
	v_mov_b32_e32 v109, v37
	s_cbranch_scc0 .LBB0_758

; #define RP_UNPK(V_, H_) ((H_) ? (f32x4){bflo((V_)[2]), bfhi((V_)[2]), bflo((V_)[3]), bfhi((V_)[3])} : (f32x4){bflo((V_)[0]), bfhi((V_)[0]), bflo((V_)[1]), bfhi((V_)[1])})
; template <int MODE, bool FIRSTX>
; __device__ __forceinline__ void row_pass(Frame& F, int layer, bool final_out, int row0) {
;     ...
;         f32x4 v[4];
; #pragma unroll
;         for (int q = 0; q < 4; ++q) v[q] = FIRSTX ? xf[q] : RP_UNPK(xb[q >> 1], q & 1);
;         if (MODE != 0) {
; #pragma unroll
;             for (int q = 0; q < 4; ++q) { f32x4 y = (f32x4){0.f, 0.f, 0.f, 0.f};
; #pragma unroll
;                 for (int k = 0; k < NY; ++k) { if (MODE == 2) { const unsigned w8 = yb[k][q >> 1][q & 1]; const f32x2 lo = __builtin_amdgcn_cvt_pk_f32_fp8((int)w8, false), hi = __builtin_amdgcn_cvt_pk_f32_fp8((int)w8, true); y += (f32x4){lo.x, lo.y, hi.x, hi.y}; }
;                                                 else y += RP_UNPK(yb[k][q >> 1], q & 1); }
;                 if (MODE == 2) y = y * (1.0f / YK8_SCALE);
;                 v[q] = v[q] * DN_ALPHA + gt[q] * y; }
;             float s = 0.f;
; #pragma unroll
;             for (int q = 0; q < 4; ++q) s += (v[q][0] + v[q][1]) + (v[q][2] + v[q][3]);
;             const float mean = wave_sum(s) * (1.0f / DM); float qq = 0.f;
; #pragma unroll
;             for (int q = 0; q < 4; ++q) { v[q] = v[q] - mean; qq += (v[q][0] * v[q][0] + v[q][1] * v[q][1]) + (v[q][2] * v[q][2] + v[q][3] * v[q][3]); }
;             const float rstd = 1.0f / sqrtf(wave_sum(qq) * (1.0f / DM) + LN_EPS);
.Lrp1f_common:
	v_lshlrev_b32_e32 v138, 16, v122
	v_and_b32_e32 v139, 0xffff0000, v122
	v_lshlrev_b32_e32 v122, 16, v123
	v_and_b32_e32 v123, 0xffff0000, v123
	v_pk_add_f32 v[122:123], v[122:123], 0 op_sel_hi:[1,0]
	v_pk_add_f32 v[138:139], v[138:139], 0 op_sel_hi:[1,0]
	v_pk_mul_f32 v[122:123], v[122:123], v[40:41]
	v_pk_mul_f32 v[138:139], v[138:139], v[38:39]
	v_pk_fma_f32 v[122:123], v[128:129], s[62:63], v[122:123] op_sel_hi:[1,0,1]
	v_lshlrev_b32_e32 v128, 16, v124
	v_and_b32_e32 v129, 0xffff0000, v124
	v_lshlrev_b32_e32 v124, 16, v125
	v_and_b32_e32 v125, 0xffff0000, v125
	v_pk_add_f32 v[124:125], v[124:125], 0 op_sel_hi:[1,0]
	v_pk_add_f32 v[128:129], v[128:129], 0 op_sel_hi:[1,0]
	v_pk_mul_f32 v[124:125], v[124:125], v[36:37]
	v_pk_fma_f32 v[126:127], v[126:127], s[62:63], v[138:139] op_sel_hi:[1,0,1]
	v_pk_fma_f32 v[120:121], v[120:121], s[62:63], v[124:125] op_sel_hi:[1,0,1]
	v_lshlrev_b32_e32 v124, 16, v114
	v_and_b32_e32 v125, 0xffff0000, v114
	v_lshlrev_b32_e32 v114, 16, v115
	v_and_b32_e32 v115, 0xffff0000, v115
	v_pk_add_f32 v[114:115], v[114:115], 0 op_sel_hi:[1,0]
	v_pk_mul_f32 v[128:129], v[128:129], v[34:35]
	v_pk_mul_f32 v[114:115], v[114:115], v[64:65]
	v_pk_fma_f32 v[118:119], v[118:119], s[62:63], v[128:129] op_sel_hi:[1,0,1]
	v_pk_fma_f32 v[112:113], v[112:113], s[62:63], v[114:115] op_sel_hi:[1,0,1]
	v_lshlrev_b32_e32 v114, 16, v116
	v_and_b32_e32 v115, 0xffff0000, v116
	v_lshlrev_b32_e32 v116, 16, v117
	v_and_b32_e32 v117, 0xffff0000, v117
	v_pk_add_f32 v[114:115], v[114:115], 0 op_sel_hi:[1,0]
	v_pk_add_f32 v[116:117], v[116:117], 0 op_sel_hi:[1,0]
	v_pk_mul_f32 v[114:115], v[114:115], v[54:55]
	v_pk_add_f32 v[124:125], v[124:125], 0 op_sel_hi:[1,0]
	v_pk_mul_f32 v[116:117], v[116:117], v[56:57]
	v_pk_fma_f32 v[106:107], v[106:107], s[62:63], v[114:115] op_sel_hi:[1,0,1]
	v_add_f32_e32 v114, v126, v127
	v_add_f32_e32 v115, v122, v123
	v_pk_mul_f32 v[124:125], v[124:125], v[62:63]
	v_pk_fma_f32 v[108:109], v[108:109], s[62:63], v[116:117] op_sel_hi:[1,0,1]
	v_add_f32_e32 v114, v114, v115
	v_add_f32_e32 v115, v118, v119
	v_add_f32_e32 v116, v120, v121
	v_pk_fma_f32 v[110:111], v[110:111], s[62:63], v[124:125] op_sel_hi:[1,0,1]
	v_add_f32_e32 v114, 0, v114
	v_add_f32_e32 v115, v115, v116
	v_add_f32_e32 v114, v115, v114
	v_add_f32_e32 v115, v110, v111
	v_add_f32_e32 v116, v112, v113
	v_add_f32_e32 v115, v115, v116
	v_add_f32_e32 v114, v115, v114
	v_add_f32_e32 v115, v106, v107
	v_add_f32_e32 v116, v108, v109
	v_add_f32_e32 v115, v115, v116
	v_add_f32_e32 v114, v115, v114
	s_nop 1
	v_add_f32_dpp v114, v114, v114 quad_perm:[1,0,3,2] row_mask:0xf bank_mask:0xf
	s_add_u32 s76, s76, 1
	s_addc_u32 s77, s77, 0
	s_nop 1
	v_add_f32_dpp v114, v114, v114 quad_perm:[2,3,0,1] row_mask:0xf bank_mask:0xf
	s_nop 1
	v_add_f32_dpp v114, v114, v114 row_half_mirror row_mask:0xf bank_mask:0xf
	s_nop 1
	v_add_f32_dpp v114, v114, v114 row_mirror row_mask:0xf bank_mask:0xf
	s_waitcnt lgkmcnt(0)
	ds_swizzle_b32 v115, v114 offset:swizzle(SWAP,16)
	s_waitcnt lgkmcnt(0)
	v_add_f32_e32 v114, v114, v115
	v_mov_b32_e32 v115, v114
	s_nop 1
	v_permlane32_swap_b32_e32 v114, v115
	v_add_f32_e32 v114, v114, v115
	v_fmac_f32_e32 v123, 0xba800000, v114
	v_fmac_f32_e32 v127, 0xba800000, v114
	v_fmamk_f32 v122, v114, 0xba800000, v122
	v_fmamk_f32 v126, v114, 0xba800000, v126
	v_mul_f32_e32 v115, v127, v127
	v_mul_f32_e32 v116, v123, v123
	v_fmac_f32_e32 v115, v126, v126
	v_fmac_f32_e32 v116, v122, v122
	v_fmac_f32_e32 v121, 0xba800000, v114
	v_fmac_f32_e32 v119, 0xba800000, v114
	v_add_f32_e32 v115, v115, v116
	v_fmamk_f32 v120, v114, 0xba800000, v120
	v_fmamk_f32 v118, v114, 0xba800000, v118
	v_mul_f32_e32 v116, v119, v119
	v_mul_f32_e32 v117, v121, v121
	v_fmac_f32_e32 v116, v118, v118
	v_fmac_f32_e32 v117, v120, v120
	v_add_f32_e32 v116, v116, v117
	v_fmac_f32_e32 v113, 0xba800000, v114
	v_fmac_f32_e32 v111, 0xba800000, v114
	v_add_f32_e32 v115, v115, v116
	v_fmamk_f32 v112, v114, 0xba800000, v112
	v_fmamk_f32 v110, v114, 0xba800000, v110
	v_mul_f32_e32 v116, v111, v111
	v_mul_f32_e32 v117, v113, v113
	v_fmac_f32_e32 v116, v110, v110
	v_fmac_f32_e32 v117, v112, v112
	v_add_f32_e32 v116, v116, v117
	v_fmac_f32_e32 v109, 0xba800000, v114
	v_fmac_f32_e32 v107, 0xba800000, v114
	v_add_f32_e32 v115, v116, v115
	v_fmamk_f32 v108, v114, 0xba800000, v108
	v_fmamk_f32 v106, v114, 0xba800000, v106
	v_mul_f32_e32 v114, v107, v107
	v_mul_f32_e32 v116, v109, v109
	v_fmac_f32_e32 v114, v106, v106
	v_fmac_f32_e32 v116, v108, v108
	v_add_f32_e32 v114, v114, v116
	v_add_f32_e32 v114, v114, v115
	s_nop 1
	v_add_f32_dpp v114, v114, v114 quad_perm:[1,0,3,2] row_mask:0xf bank_mask:0xf
	s_nop 1
	v_add_f32_dpp v114, v114, v114 quad_perm:[2,3,0,1] row_mask:0xf bank_mask:0xf
	s_nop 1
	v_add_f32_dpp v114, v114, v114 row_half_mirror row_mask:0xf bank_mask:0xf
	s_nop 1
	v_add_f32_dpp v114, v114, v114 row_mirror row_mask:0xf bank_mask:0xf
	s_waitcnt lgkmcnt(0)
	ds_swizzle_b32 v115, v114 offset:swizzle(SWAP,16)
	s_waitcnt lgkmcnt(0)
; __device__ __forceinline__ unsigned pk2(float lo, float hi) { return f2bf(lo) | (f2bf(hi) << 16); }
; __device__ __forceinline__ unsigned cvt_fp8x4(float a, float b, float c, float d) { int w = __builtin_amdgcn_cvt_pk_fp8_f32(a, b, 0, false); w = __builtin_amdgcn_cvt_pk_fp8_f32(c, d, w, true); return (unsigned)w; }
; template <int MODE, bool FIRSTX>
; __device__ __forceinline__ void row_pass(Frame& F, int layer, bool final_out, int row0) {
;     ...
;             const float rstd = 1.0f / sqrtf(wave_sum(qq) * (1.0f / DM) + LN_EPS);
; #pragma unroll
;             for (int q = 0; q < 4; ++q) v[q] = v[q] * rstd * lg[q] + lb[q];
;             if (final_out) { if (row >= NCTX) {
; #pragma unroll
;                 for (int q = 0; q < 4; ++q) *(f32x4*)(F.out + (size_t)(row - NCTX) * DM + RP_COL(q)) = v[q]; } }
;             else {
; #pragma unroll
;                 for (int j = 0; j < 2; ++j) { u32x4 w; w.x = pk2(v[2 * j][0], v[2 * j][1]); w.y = pk2(v[2 * j][2], v[2 * j][3]); w.z = pk2(v[2 * j + 1][0], v[2 * j + 1][1]); w.w = pk2(v[2 * j + 1][2], v[2 * j + 1][3]);
;                     *(u32x4*)(X + (size_t)row * DM + lc + 512 * j) = w; } }
;         }
;         if (!final_out) {
; #pragma unroll
;             for (int j = 0; j < 2; ++j) { const f32x4 h0 = v[2 * j] * (sc[2 * j] + 1.0f) + sh[2 * j], h1 = v[2 * j + 1] * (sc[2 * j + 1] + 1.0f) + sh[2 * j + 1];
;                 if (MODE == 1 || (nlayer % 3) == 2) { u32x4 w; w.x = pk2(h0[0], h0[1]); w.y = pk2(h0[2], h0[3]); w.z = pk2(h1[0], h1[1]); w.w = pk2(h1[2], h1[3]);
;                     *(u32x4*)(H + (size_t)row * DM + lc + 512 * j) = w; }
;                 if (MODE == 1 || (nlayer % 3) != 2) {                                u32x2 w8; w8.x = cvt_fp8x4(h0[0], h0[1], h0[2], h0[3]); w8.y = cvt_fp8x4(h1[0], h1[1], h1[2], h1[3]); *(u32x2*)(F.ws + WS_H8 + (size_t)row * DM + lc + 512 * j) = w8; } }
	v_add_f32_e32 v114, v114, v115
	v_mov_b32_e32 v115, v114
	s_nop 1
	v_permlane32_swap_b32_e32 v114, v115
	v_add_f32_e32 v114, v114, v115
	v_fmamk_f32 v114, v114, 0x3a800000, v188
	v_mul_f32_e32 v115, 0x4f800000, v114
	v_cmp_gt_f32_e32 vcc, s31, v114
	s_nop 1
	v_cndmask_b32_e32 v114, v114, v115, vcc
	v_sqrt_f32_e32 v115, v114
	s_nop 0
	v_add_u32_e32 v116, -1, v115
	v_fma_f32 v117, -v116, v115, v114
	v_cmp_ge_f32_e64 s[2:3], 0, v117
	v_add_u32_e32 v117, 1, v115
	s_nop 0
	v_cndmask_b32_e64 v116, v115, v116, s[2:3]
	v_fma_f32 v115, -v117, v115, v114
	v_cmp_lt_f32_e64 s[2:3], 0, v115
	s_nop 1
	v_cndmask_b32_e64 v115, v116, v117, s[2:3]
	v_mul_f32_e32 v116, 0x37800000, v115
	v_cndmask_b32_e32 v115, v115, v116, vcc
	v_cmp_class_f32_e32 vcc, v114, v189
	s_nop 1
	v_cndmask_b32_e32 v114, v115, v114, vcc
	v_div_scale_f32 v115, s[0:1], v114, v114, 1.0
	v_rcp_f32_e32 v116, v115
	s_add_i32 s0, s4, s76
	s_add_u32 s60, s60, 0x1000
	s_addc_u32 s61, s61, 0
	v_fma_f32 v117, -v115, v116, 1.0
	v_fmac_f32_e32 v116, v117, v116
	v_div_scale_f32 v117, vcc, 1.0, v114, 1.0
	v_mul_f32_e32 v124, v117, v116
	v_fma_f32 v125, -v115, v124, v117
	v_fmac_f32_e32 v124, v125, v116
	v_fma_f32 v115, -v115, v124, v117
	v_div_fmas_f32 v115, v115, v116, v124
	v_div_fixup_f32 v114, v115, v114, 1.0
	v_pk_mul_f32 v[116:117], v[126:127], v[114:115] op_sel_hi:[1,0]
	v_pk_mul_f32 v[106:107], v[106:107], v[114:115] op_sel_hi:[1,0]
	v_pk_fma_f32 v[116:117], v[2:3], v[116:117], v[6:7]
	v_pk_mul_f32 v[122:123], v[122:123], v[114:115] op_sel_hi:[1,0]
	v_pk_mul_f32 v[118:119], v[118:119], v[114:115] op_sel_hi:[1,0]
	v_pk_mul_f32 v[120:121], v[120:121], v[114:115] op_sel_hi:[1,0]
	v_pk_mul_f32 v[110:111], v[110:111], v[114:115] op_sel_hi:[1,0]
	v_pk_mul_f32 v[112:113], v[112:113], v[114:115] op_sel_hi:[1,0]
	v_pk_mul_f32 v[108:109], v[108:109], v[114:115] op_sel_hi:[1,0]
	v_pk_fma_f32 v[114:115], v[26:27], v[106:107], v[30:31]
	v_bfe_u32 v106, v116, 16, 1
	v_add3_u32 v106, v116, v106, s43
	v_bfe_u32 v107, v117, 16, 1
	v_pk_fma_f32 v[122:123], v[4:5], v[122:123], v[8:9]
	v_lshrrev_b32_e32 v106, 16, v106
	v_add3_u32 v107, v117, v107, s43
	v_and_or_b32 v106, v107, s33, v106
	v_bfe_u32 v107, v122, 16, 1
	v_pk_fma_f32 v[124:125], v[28:29], v[108:109], v[32:33]
	v_add3_u32 v107, v122, v107, s43
	v_bfe_u32 v108, v123, 16, 1
	v_pk_fma_f32 v[118:119], v[10:11], v[118:119], v[14:15]
	v_lshrrev_b32_e32 v107, 16, v107
	v_add3_u32 v108, v123, v108, s43
	v_and_or_b32 v107, v108, s33, v107
	v_bfe_u32 v108, v118, 16, 1
	v_add3_u32 v108, v118, v108, s43
	v_bfe_u32 v109, v119, 16, 1
	v_pk_fma_f32 v[120:121], v[12:13], v[120:121], v[16:17]
	v_lshrrev_b32_e32 v108, 16, v108
	v_add3_u32 v109, v119, v109, s43
	v_and_or_b32 v108, v109, s33, v108
	v_bfe_u32 v109, v120, 16, 1
	v_add3_u32 v109, v120, v109, s43
	v_bfe_u32 v128, v121, 16, 1
	v_lshl_add_u64 v[126:127], s[74:75], 0, v[132:133]
	v_lshrrev_b32_e32 v109, 16, v109
	v_add3_u32 v128, v121, v128, s43
	v_and_or_b32 v109, v128, s33, v109
	v_add_co_u32_e32 v128, vcc, s39, v126
	v_pk_fma_f32 v[110:111], v[18:19], v[110:111], v[22:23]
	s_nop 0
	v_addc_co_u32_e32 v129, vcc, 0, v127, vcc
	global_store_dwordx4 v[128:129], v[106:109], off
	v_pk_fma_f32 v[112:113], v[20:21], v[112:113], v[24:25]
	v_bfe_u32 v137, v125, 16, 1
	v_bfe_u32 v106, v110, 16, 1
	v_add3_u32 v106, v110, v106, s43
	v_bfe_u32 v107, v111, 16, 1
	v_lshrrev_b32_e32 v106, 16, v106
	v_add3_u32 v107, v111, v107, s43
	v_and_or_b32 v106, v107, s33, v106
	v_bfe_u32 v107, v112, 16, 1
	v_add3_u32 v107, v112, v107, s43
	v_bfe_u32 v108, v113, 16, 1
	v_lshrrev_b32_e32 v107, 16, v107
	v_add3_u32 v108, v113, v108, s43
	v_and_or_b32 v107, v108, s33, v107
	v_bfe_u32 v108, v114, 16, 1
	v_add3_u32 v108, v114, v108, s43
	v_bfe_u32 v109, v115, 16, 1
	v_lshrrev_b32_e32 v108, 16, v108
	v_add3_u32 v109, v115, v109, s43
	v_and_or_b32 v108, v109, s33, v108
	v_bfe_u32 v109, v124, 16, 1
	v_add3_u32 v109, v124, v109, s43
	v_lshrrev_b32_e32 v109, 16, v109
	v_add3_u32 v137, v125, v137, s43
	v_and_or_b32 v109, v137, s33, v109
	global_store_dwordx4 v[128:129], v[106:109], off offset:1024
	v_lshl_add_u64 v[132:133], v[132:133], 0, s[50:51]
	s_cmp_ge_i32 s0, s11
	v_pk_add_f32 v[106:107], v[60:61], 1.0 op_sel_hi:[1,0]
	v_pk_add_f32 v[108:109], v[58:59], 1.0 op_sel_hi:[1,0]
	v_pk_fma_f32 v[122:123], v[106:107], v[122:123], v[48:49]
	v_pk_fma_f32 v[116:117], v[108:109], v[116:117], v[46:47]
	v_pk_add_f32 v[106:107], v[52:53], 1.0 op_sel_hi:[1,0]
	v_pk_add_f32 v[108:109], v[50:51], 1.0 op_sel_hi:[1,0]
	v_pk_fma_f32 v[120:121], v[106:107], v[120:121], v[44:45]
	v_and_b32_sdwa v107, v116, v185 dst_sel:DWORD dst_unused:UNUSED_PAD src0_sel:WORD_1 src1_sel:DWORD
	v_pk_fma_f32 v[118:119], v[108:109], v[118:119], v[42:43]
	v_add3_u32 v108, v116, v107, s43
	v_and_b32_sdwa v107, v123, v185 dst_sel:DWORD dst_unused:UNUSED_PAD src0_sel:WORD_1 src1_sel:DWORD
	v_and_b32_sdwa v109, v117, v185 dst_sel:DWORD dst_unused:UNUSED_PAD src0_sel:WORD_1 src1_sel:DWORD
; __device__ __forceinline__ unsigned pk2(float lo, float hi) { return f2bf(lo) | (f2bf(hi) << 16); }
; __device__ __forceinline__ unsigned cvt_fp8x4(float a, float b, float c, float d) { int w = __builtin_amdgcn_cvt_pk_fp8_f32(a, b, 0, false); w = __builtin_amdgcn_cvt_pk_fp8_f32(c, d, w, true); return (unsigned)w; }
; template <int MODE, bool FIRSTX>
; __device__ __forceinline__ void row_pass(Frame& F, int layer, bool final_out, int row0) {
;     ...
;         if (!final_out) {
; #pragma unroll
;             for (int j = 0; j < 2; ++j) { const f32x4 h0 = v[2 * j] * (sc[2 * j] + 1.0f) + sh[2 * j], h1 = v[2 * j + 1] * (sc[2 * j + 1] + 1.0f) + sh[2 * j + 1];
;                 if (MODE == 1 || (nlayer % 3) == 2) { u32x4 w; w.x = pk2(h0[0], h0[1]); w.y = pk2(h0[2], h0[3]); w.z = pk2(h1[0], h1[1]); w.w = pk2(h1[2], h1[3]);
;                     *(u32x4*)(H + (size_t)row * DM + lc + 512 * j) = w; }
;                 if (MODE == 1 || (nlayer % 3) != 2) {                                u32x2 w8; w8.x = cvt_fp8x4(h0[0], h0[1], h0[2], h0[3]); w8.y = cvt_fp8x4(h1[0], h1[1], h1[2], h1[3]); *(u32x2*)(F.ws + WS_H8 + (size_t)row * DM + lc + 512 * j) = w8; } }
;         }
; #pragma unroll
;         for (int q = 0; q < 4; ++q) xf[q] = xfn[q];
; #pragma unroll
;         for (int j = 0; j < 2; ++j) { xb[j] = xbn[j];
; #pragma unroll
;             for (int k = 0; k < (NY ? NY : 1); ++k) yb[k][j] = ybn[k][j]; }
	v_and_b32_sdwa v106, v122, v185 dst_sel:DWORD dst_unused:UNUSED_PAD src0_sel:WORD_1 src1_sel:DWORD
	v_add3_u32 v107, v123, v107, s43
	v_add3_u32 v109, v117, v109, s43
	v_add3_u32 v106, v122, v106, s43
	v_and_b32_e32 v107, 0xffff0000, v107
	v_and_b32_e32 v109, 0xffff0000, v109
	v_or_b32_sdwa v107, v107, v106 dst_sel:DWORD dst_unused:UNUSED_PAD src0_sel:DWORD src1_sel:WORD_1
	v_or_b32_sdwa v106, v109, v108 dst_sel:DWORD dst_unused:UNUSED_PAD src0_sel:DWORD src1_sel:WORD_1
	v_and_b32_sdwa v109, v118, v185 dst_sel:DWORD dst_unused:UNUSED_PAD src0_sel:WORD_1 src1_sel:DWORD
	v_add3_u32 v128, v118, v109, s43
	v_and_b32_sdwa v109, v121, v185 dst_sel:DWORD dst_unused:UNUSED_PAD src0_sel:WORD_1 src1_sel:DWORD
	v_and_b32_sdwa v129, v119, v185 dst_sel:DWORD dst_unused:UNUSED_PAD src0_sel:WORD_1 src1_sel:DWORD
	v_and_b32_sdwa v108, v120, v185 dst_sel:DWORD dst_unused:UNUSED_PAD src0_sel:WORD_1 src1_sel:DWORD
	v_add3_u32 v109, v121, v109, s43
	v_add3_u32 v129, v119, v129, s43
	v_add3_u32 v108, v120, v108, s43
	v_and_b32_e32 v109, 0xffff0000, v109
	v_and_b32_e32 v129, 0xffff0000, v129
	v_or_b32_sdwa v109, v109, v108 dst_sel:DWORD dst_unused:UNUSED_PAD src0_sel:DWORD src1_sel:WORD_1
	v_or_b32_sdwa v108, v129, v128 dst_sel:DWORD dst_unused:UNUSED_PAD src0_sel:DWORD src1_sel:WORD_1
	v_mov_b32_e32 v128, v1
	v_cvt_pk_fp8_f32 v128, v116, v117
	v_add_co_u32_e32 v116, vcc, s28, v126
	v_mov_b32_e32 v129, v1
	s_nop 0
	v_addc_co_u32_e32 v117, vcc, 0, v127, vcc
	v_cvt_pk_fp8_f32 v129, v118, v119
	global_store_dwordx4 v[116:117], v[106:109], off
	v_cvt_pk_fp8_f32 v128, v122, v123 op_sel:[0,0,1]
	v_cvt_pk_fp8_f32 v129, v120, v121 op_sel:[0,0,1]
	v_lshl_add_u64 v[106:107], s[74:75], 0, v[134:135]
	v_add_co_u32_e32 v118, vcc, s38, v106
	v_pk_add_f32 v[108:109], v[78:79], 1.0 op_sel_hi:[1,0]
	s_nop 0
	v_addc_co_u32_e32 v119, vcc, 0, v107, vcc
	v_pk_add_f32 v[106:107], v[80:81], 1.0 op_sel_hi:[1,0]
	v_pk_fma_f32 v[108:109], v[108:109], v[110:111], v[70:71]
	v_pk_fma_f32 v[112:113], v[106:107], v[112:113], v[72:73]
	v_pk_add_f32 v[106:107], v[76:77], 1.0 op_sel_hi:[1,0]
	v_pk_add_f32 v[110:111], v[74:75], 1.0 op_sel_hi:[1,0]
	v_pk_fma_f32 v[120:121], v[106:107], v[124:125], v[68:69]
	v_and_b32_sdwa v107, v108, v185 dst_sel:DWORD dst_unused:UNUSED_PAD src0_sel:WORD_1 src1_sel:DWORD
	v_pk_fma_f32 v[110:111], v[110:111], v[114:115], v[66:67]
	v_add3_u32 v114, v108, v107, s43
	v_and_b32_sdwa v107, v113, v185 dst_sel:DWORD dst_unused:UNUSED_PAD src0_sel:WORD_1 src1_sel:DWORD
	v_and_b32_sdwa v115, v109, v185 dst_sel:DWORD dst_unused:UNUSED_PAD src0_sel:WORD_1 src1_sel:DWORD
	v_and_b32_sdwa v106, v112, v185 dst_sel:DWORD dst_unused:UNUSED_PAD src0_sel:WORD_1 src1_sel:DWORD
	v_add3_u32 v107, v113, v107, s43
	v_add3_u32 v115, v109, v115, s43
	v_add3_u32 v106, v112, v106, s43
	v_and_b32_e32 v107, 0xffff0000, v107
	v_and_b32_e32 v115, 0xffff0000, v115
	v_or_b32_sdwa v107, v107, v106 dst_sel:DWORD dst_unused:UNUSED_PAD src0_sel:DWORD src1_sel:WORD_1
	v_or_b32_sdwa v106, v115, v114 dst_sel:DWORD dst_unused:UNUSED_PAD src0_sel:DWORD src1_sel:WORD_1
	v_and_b32_sdwa v114, v120, v185 dst_sel:DWORD dst_unused:UNUSED_PAD src0_sel:WORD_1 src1_sel:DWORD
	v_and_b32_sdwa v115, v110, v185 dst_sel:DWORD dst_unused:UNUSED_PAD src0_sel:WORD_1 src1_sel:DWORD
	v_add3_u32 v122, v110, v115, s43
	v_add3_u32 v123, v120, v114, s43
	v_and_b32_sdwa v114, v121, v185 dst_sel:DWORD dst_unused:UNUSED_PAD src0_sel:WORD_1 src1_sel:DWORD
	v_and_b32_sdwa v115, v111, v185 dst_sel:DWORD dst_unused:UNUSED_PAD src0_sel:WORD_1 src1_sel:DWORD
	v_add3_u32 v124, v121, v114, s43
	v_add3_u32 v125, v111, v115, s43
	v_mov_b32_e32 v114, v1
	v_mov_b32_e32 v115, v1
	v_cvt_pk_fp8_f32 v114, v108, v109
	v_cvt_pk_fp8_f32 v115, v110, v111
	v_and_b32_e32 v108, 0xffff0000, v124
	v_and_b32_e32 v110, 0xffff0000, v125
	v_cvt_pk_fp8_f32 v114, v112, v113 op_sel:[0,0,1]
	v_cvt_pk_fp8_f32 v115, v120, v121 op_sel:[0,0,1]
	v_or_b32_sdwa v109, v108, v123 dst_sel:DWORD dst_unused:UNUSED_PAD src0_sel:DWORD src1_sel:WORD_1
	v_or_b32_sdwa v108, v110, v122 dst_sel:DWORD dst_unused:UNUSED_PAD src0_sel:DWORD src1_sel:WORD_1
	global_store_dwordx2 v[118:119], v[128:129], off
	global_store_dwordx4 v[116:117], v[106:109], off offset:1024
	global_store_dwordx2 v[118:119], v[114:115], off offset:512
	s_waitcnt vmcnt(6)
	v_mov_b64_e32 v[112:113], v[96:97]
	v_mov_b64_e32 v[108:109], v[92:93]
	v_mov_b64_e32 v[120:121], v[84:85]
	v_mov_b64_e32 v[128:129], v[88:89]
	v_lshl_add_u64 v[134:135], v[134:135], 0, s[54:55]
	v_mov_b64_e32 v[106:107], v[90:91]
	v_mov_b64_e32 v[110:111], v[94:95]
	v_mov_b64_e32 v[118:119], v[82:83]
	v_mov_b64_e32 v[126:127], v[86:87]
	v_mov_b32_e32 v122, v98
	v_mov_b32_e32 v123, v99
	v_mov_b32_e32 v124, v100
	v_mov_b32_e32 v125, v101
	v_mov_b32_e32 v114, v102
	v_mov_b32_e32 v115, v103
	v_mov_b32_e32 v116, v104
	v_mov_b32_e32 v117, v105
	s_cbranch_scc1 .LBB0_777

; #define PG8_BAR __builtin_amdgcn_s_barrier()
; template <class Epi, class Sched, bool ALIGN_EPI, bool FP8 = false>
; __device__ __forceinline__ void gemm_phase(LAS unsigned char* lds, const bf16_t* A, const bf16_t* Bt, const int K, const Sched& S, const Epi& E, const int wave_in) {
;     ...
;         if (!has_next) break;
; #pragma unroll
;         for (int a = 0; a < 2; ++a)
; #pragma unroll
;             for (int b = 0; b < 2; ++b)
; #pragma unroll
;                 for (int m = 0; m < 4; ++m)
; #pragma unroll
;                     for (int n = 0; n < 2; ++n) acc[a][b][m][n] = (f32x4){0.f, 0.f, 0.f, 0.f};
;         cur = nxt; cB = nB; ++ui;
; #pragma unroll
;         for (int h = 0; h < 2; ++h)
; #pragma unroll
;             for (int i = 0; i < 2; ++i) vA[h][i] = vN[h][i];
;         if constexpr (ALIGN_EPI) { if (wr == 1) PG8_BAR; }
.LBB0_1051:
	s_add_u32 s1, s10, 0x100
	v_mov_b32_e32 v34, 0
	s_addc_u32 s27, s11, 0
	s_mov_b32 s95, -2
	s_mov_b64 s[80:81], s[60:61]
	v_mov_b32_e32 v35, 0
	v_mov_b64_e32 v[36:37], 0
	v_mov_b64_e32 v[42:43], 0
	v_mov_b64_e32 v[44:45], 0
	v_mov_b64_e32 v[50:51], 0
	v_mov_b64_e32 v[52:53], 0
	v_mov_b64_e32 v[58:59], 0
	v_mov_b64_e32 v[60:61], 0
	v_mov_b64_e32 v[66:67], 0
	v_mov_b64_e32 v[68:69], 0
	v_mov_b64_e32 v[74:75], 0
	v_mov_b64_e32 v[76:77], 0
	v_mov_b64_e32 v[82:83], 0
	v_mov_b64_e32 v[84:85], 0
	v_mov_b64_e32 v[90:91], 0
	v_mov_b64_e32 v[92:93], 0
	v_mov_b64_e32 v[38:39], 0
	v_mov_b64_e32 v[40:41], 0
	v_mov_b64_e32 v[46:47], 0
	v_mov_b64_e32 v[48:49], 0
	v_mov_b64_e32 v[54:55], 0
	v_mov_b64_e32 v[56:57], 0
	v_mov_b64_e32 v[62:63], 0
	v_mov_b64_e32 v[64:65], 0
	v_mov_b64_e32 v[70:71], 0
	v_mov_b64_e32 v[72:73], 0
	v_mov_b64_e32 v[78:79], 0
	v_mov_b64_e32 v[80:81], 0
	v_mov_b64_e32 v[86:87], 0
	v_mov_b64_e32 v[88:89], 0
	v_mov_b64_e32 v[94:95], 0
	v_mov_b64_e32 v[96:97], 0
	v_mov_b64_e32 v[98:99], 0
	v_mov_b64_e32 v[100:101], 0
	v_mov_b64_e32 v[106:107], 0
	v_mov_b64_e32 v[108:109], 0
	v_mov_b64_e32 v[114:115], 0
	v_mov_b64_e32 v[116:117], 0
	v_mov_b64_e32 v[122:123], 0
	v_mov_b64_e32 v[124:125], 0
	v_mov_b64_e32 v[130:131], 0
	v_mov_b64_e32 v[132:133], 0
	v_mov_b64_e32 v[138:139], 0
	v_mov_b64_e32 v[140:141], 0
	v_mov_b64_e32 v[148:149], 0
	v_mov_b64_e32 v[150:151], 0
	v_mov_b64_e32 v[156:157], 0
	v_mov_b64_e32 v[158:159], 0
	v_mov_b64_e32 v[102:103], 0
	v_mov_b64_e32 v[104:105], 0
	v_mov_b64_e32 v[110:111], 0
	v_mov_b64_e32 v[112:113], 0
	v_mov_b64_e32 v[118:119], 0
	v_mov_b64_e32 v[120:121], 0
	v_mov_b64_e32 v[126:127], 0
	v_mov_b64_e32 v[128:129], 0
	v_mov_b64_e32 v[134:135], 0
	v_mov_b64_e32 v[136:137], 0
	v_mov_b64_e32 v[142:143], 0
	v_mov_b64_e32 v[144:145], 0
	v_mov_b64_e32 v[152:153], 0
	v_mov_b64_e32 v[154:155], 0
	v_mov_b64_e32 v[160:161], 0
	v_mov_b64_e32 v[162:163], 0
	s_branch .LBB0_1053
	s_nop 0
	s_nop 0
	s_nop 0
	s_nop 0

; #define RP_UNPK(V_, H_) ((H_) ? (f32x4){bflo((V_)[2]), bfhi((V_)[2]), bflo((V_)[3]), bfhi((V_)[3])} : (f32x4){bflo((V_)[0]), bfhi((V_)[0]), bflo((V_)[1]), bfhi((V_)[1])})
; template <int MODE, bool FIRSTX>
; __device__ __forceinline__ void row_pass(Frame& F, int layer, bool final_out, int row0) {
;     ...
;         if (MODE != 0) {
; #pragma unroll
;             for (int q = 0; q < 4; ++q) { f32x4 y = (f32x4){0.f, 0.f, 0.f, 0.f};
; #pragma unroll
;                 for (int k = 0; k < NY; ++k) { if (MODE == 2) { const unsigned w8 = yb[k][q >> 1][q & 1]; const f32x2 lo = __builtin_amdgcn_cvt_pk_f32_fp8((int)w8, false), hi = __builtin_amdgcn_cvt_pk_f32_fp8((int)w8, true); y += (f32x4){lo.x, lo.y, hi.x, hi.y}; }
;                                                 else y += RP_UNPK(yb[k][q >> 1], q & 1); }
;                 if (MODE == 2) y = y * (1.0f / YK8_SCALE);
;                 v[q] = v[q] * DN_ALPHA + gt[q] * y; }
;             float s = 0.f;
; #pragma unroll
;             for (int q = 0; q < 4; ++q) s += (v[q][0] + v[q][1]) + (v[q][2] + v[q][3]);
;             const float mean = wave_sum(s) * (1.0f / DM); float qq = 0.f;
; #pragma unroll
;             for (int q = 0; q < 4; ++q) { v[q] = v[q] - mean; qq += (v[q][0] * v[q][0] + v[q][1] * v[q][1]) + (v[q][2] * v[q][2] + v[q][3] * v[q][3]); }
;             const float rstd = 1.0f / sqrtf(wave_sum(qq) * (1.0f / DM) + LN_EPS);
.LBB0_1210:
	v_lshlrev_b32_e32 v154, 16, v96
	v_and_b32_e32 v155, 0xffff0000, v96
	v_lshlrev_b32_e32 v156, 16, v97
	v_and_b32_e32 v157, 0xffff0000, v97
	v_lshlrev_b32_e32 v158, 16, v90
	v_and_b32_e32 v159, 0xffff0000, v90
	v_lshlrev_b32_e32 v160, 16, v91
	v_and_b32_e32 v161, 0xffff0000, v91
	v_lshlrev_b32_e32 v96, 16, v92
	v_and_b32_e32 v97, 0xffff0000, v92
	v_lshlrev_b32_e32 v150, 16, v93
	v_and_b32_e32 v151, 0xffff0000, v93
	v_cvt_pk_f32_fp8_e32 v[90:91], v142
	v_cvt_pk_f32_fp8_sdwa v[92:93], v142 src0_sel:WORD_1
	v_cvt_pk_f32_fp8_e32 v[162:163], v140
	v_cvt_pk_f32_fp8_sdwa v[164:165], v140 src0_sel:WORD_1
	v_pk_add_f32 v[90:91], v[90:91], 0 op_sel_hi:[1,0]
	v_pk_add_f32 v[92:93], v[92:93], 0 op_sel_hi:[1,0]
	v_pk_add_f32 v[90:91], v[90:91], v[162:163]
	v_pk_add_f32 v[92:93], v[92:93], v[164:165]
	v_cvt_pk_f32_fp8_e32 v[162:163], v144
	v_cvt_pk_f32_fp8_sdwa v[164:165], v144 src0_sel:WORD_1
	v_lshlrev_b32_e32 v152, 16, v94
	v_and_b32_e32 v153, 0xffff0000, v94
	v_pk_add_f32 v[90:91], v[90:91], v[162:163]
	v_pk_add_f32 v[92:93], v[92:93], v[164:165]
	v_cvt_pk_f32_fp8_e32 v[162:163], v148
	v_cvt_pk_f32_fp8_sdwa v[164:165], v148 src0_sel:WORD_1
	v_lshlrev_b32_e32 v94, 16, v95
	v_and_b32_e32 v95, 0xffff0000, v95
	v_pk_add_f32 v[90:91], v[90:91], v[162:163]
	v_pk_add_f32 v[92:93], v[92:93], v[164:165]
	v_pk_mul_f32 v[90:91], v[90:91], s[70:71] op_sel_hi:[1,0]
	v_pk_mul_f32 v[92:93], v[92:93], s[70:71] op_sel_hi:[1,0]
	v_pk_mul_f32 v[162:163], v[70:71], v[90:91]
	v_pk_mul_f32 v[90:91], v[72:73], v[92:93]
	v_pk_fma_f32 v[92:93], v[152:153], s[62:63], v[162:163] op_sel_hi:[1,0,1]
	v_pk_fma_f32 v[90:91], v[94:95], s[62:63], v[90:91] op_sel_hi:[1,0,1]
	v_cvt_pk_f32_fp8_e32 v[94:95], v143
	v_cvt_pk_f32_fp8_sdwa v[142:143], v143 src0_sel:WORD_1
	v_cvt_pk_f32_fp8_e32 v[152:153], v141
	v_cvt_pk_f32_fp8_sdwa v[140:141], v141 src0_sel:WORD_1
	v_pk_add_f32 v[94:95], v[94:95], 0 op_sel_hi:[1,0]
	v_pk_add_f32 v[142:143], v[142:143], 0 op_sel_hi:[1,0]
	v_pk_add_f32 v[94:95], v[94:95], v[152:153]
	v_pk_add_f32 v[140:141], v[142:143], v[140:141]
	v_cvt_pk_f32_fp8_e32 v[142:143], v145
	v_cvt_pk_f32_fp8_sdwa v[144:145], v145 src0_sel:WORD_1
	v_cvt_pk_f32_fp8_sdwa v[152:153], v98 src0_sel:WORD_1
	v_add_f32_e32 v0, v92, v93
	v_pk_add_f32 v[94:95], v[94:95], v[142:143]
	v_cvt_pk_f32_fp8_e32 v[142:143], v149
	v_pk_add_f32 v[140:141], v[140:141], v[144:145]
	v_cvt_pk_f32_fp8_sdwa v[144:145], v149 src0_sel:WORD_1
	v_cvt_pk_f32_fp8_e32 v[148:149], v98
	v_pk_add_f32 v[94:95], v[94:95], v[142:143]
	v_pk_add_f32 v[140:141], v[140:141], v[144:145]
	v_pk_mul_f32 v[94:95], v[94:95], s[70:71] op_sel_hi:[1,0]
	v_pk_mul_f32 v[140:141], v[140:141], s[70:71] op_sel_hi:[1,0]
	v_pk_mul_f32 v[142:143], v[74:75], v[94:95]
	v_pk_mul_f32 v[94:95], v[76:77], v[140:141]
	v_pk_fma_f32 v[140:141], v[154:155], s[62:63], v[142:143] op_sel_hi:[1,0,1]
	v_cvt_pk_f32_fp8_e32 v[142:143], v100
	v_cvt_pk_f32_fp8_sdwa v[144:145], v100 src0_sel:WORD_1
	v_pk_fma_f32 v[94:95], v[156:157], s[62:63], v[94:95] op_sel_hi:[1,0,1]
	v_pk_add_f32 v[142:143], v[142:143], 0 op_sel_hi:[1,0]
	v_pk_add_f32 v[144:145], v[144:145], 0 op_sel_hi:[1,0]
	v_pk_add_f32 v[142:143], v[142:143], v[148:149]
	v_cvt_pk_f32_fp8_e32 v[148:149], v102
	v_pk_add_f32 v[144:145], v[144:145], v[152:153]
	v_cvt_pk_f32_fp8_sdwa v[152:153], v102 src0_sel:WORD_1
	v_pk_add_f32 v[142:143], v[142:143], v[148:149]
	v_cvt_pk_f32_fp8_e32 v[148:149], v104
	v_pk_add_f32 v[144:145], v[144:145], v[152:153]
	v_cvt_pk_f32_fp8_sdwa v[152:153], v104 src0_sel:WORD_1
	v_pk_add_f32 v[142:143], v[142:143], v[148:149]
	v_cvt_pk_f32_fp8_e32 v[148:149], v101
	v_cvt_pk_f32_fp8_sdwa v[100:101], v101 src0_sel:WORD_1
	v_pk_add_f32 v[144:145], v[144:145], v[152:153]
	v_cvt_pk_f32_fp8_e32 v[152:153], v99
	v_cvt_pk_f32_fp8_sdwa v[98:99], v99 src0_sel:WORD_1
	v_pk_add_f32 v[100:101], v[100:101], 0 op_sel_hi:[1,0]
	v_pk_add_f32 v[148:149], v[148:149], 0 op_sel_hi:[1,0]
	v_pk_mul_f32 v[144:145], v[144:145], s[70:71] op_sel_hi:[1,0]
	v_pk_add_f32 v[98:99], v[100:101], v[98:99]
	v_cvt_pk_f32_fp8_e32 v[100:101], v103
	v_cvt_pk_f32_fp8_sdwa v[102:103], v103 src0_sel:WORD_1
	v_pk_add_f32 v[148:149], v[148:149], v[152:153]
	v_pk_mul_f32 v[142:143], v[142:143], s[70:71] op_sel_hi:[1,0]
	v_pk_add_f32 v[100:101], v[148:149], v[100:101]
	v_pk_add_f32 v[98:99], v[98:99], v[102:103]
	v_cvt_pk_f32_fp8_e32 v[102:103], v105
	v_cvt_pk_f32_fp8_sdwa v[104:105], v105 src0_sel:WORD_1
	v_pk_mul_f32 v[142:143], v[78:79], v[142:143]
	v_pk_mul_f32 v[144:145], v[80:81], v[144:145]
	v_pk_add_f32 v[100:101], v[100:101], v[102:103]
	v_pk_add_f32 v[98:99], v[98:99], v[104:105]
	v_pk_fma_f32 v[144:145], v[160:161], s[62:63], v[144:145] op_sel_hi:[1,0,1]
	v_pk_mul_f32 v[98:99], v[98:99], s[70:71] op_sel_hi:[1,0]
	v_pk_fma_f32 v[142:143], v[158:159], s[62:63], v[142:143] op_sel_hi:[1,0,1]
	v_pk_mul_f32 v[98:99], v[88:89], v[98:99]
	v_pk_mul_f32 v[100:101], v[100:101], s[70:71] op_sel_hi:[1,0]
	v_pk_fma_f32 v[148:149], v[150:151], s[62:63], v[98:99] op_sel_hi:[1,0,1]
	v_add_f32_e32 v98, v90, v91
	v_add_f32_e32 v0, v0, v98
	v_add_f32_e32 v98, v140, v141
	v_add_f32_e32 v99, v94, v95
	v_add_f32_e32 v0, 0, v0
	v_add_f32_e32 v98, v98, v99
	v_pk_mul_f32 v[100:101], v[86:87], v[100:101]
	v_add_f32_e32 v0, v0, v98
	v_add_f32_e32 v98, v142, v143
	v_add_f32_e32 v99, v144, v145
	v_pk_fma_f32 v[96:97], v[96:97], s[62:63], v[100:101] op_sel_hi:[1,0,1]
	v_add_f32_e32 v98, v98, v99
	v_add_f32_e32 v0, v0, v98
	v_add_f32_e32 v98, v96, v97
	v_add_f32_e32 v99, v148, v149
	v_add_f32_e32 v98, v98, v99
	v_add_f32_e32 v0, v0, v98
	s_nop 1
	v_add_f32_dpp v0, v0, v0 quad_perm:[1,0,3,2] row_mask:0xf bank_mask:0xf
	s_nop 1
	v_add_f32_dpp v0, v0, v0 quad_perm:[2,3,0,1] row_mask:0xf bank_mask:0xf
	s_nop 1
	v_add_f32_dpp v0, v0, v0 row_half_mirror row_mask:0xf bank_mask:0xf
	s_nop 1
	v_add_f32_dpp v0, v0, v0 row_mirror row_mask:0xf bank_mask:0xf
	s_waitcnt lgkmcnt(0)
; __device__ __forceinline__ unsigned pk2(float lo, float hi) { return f2bf(lo) | (f2bf(hi) << 16); }
; template <int MODE, bool FIRSTX>
; __device__ __forceinline__ void row_pass(Frame& F, int layer, bool final_out, int row0) {
;     ...
;             const float mean = wave_sum(s) * (1.0f / DM); float qq = 0.f;
; #pragma unroll
;             for (int q = 0; q < 4; ++q) { v[q] = v[q] - mean; qq += (v[q][0] * v[q][0] + v[q][1] * v[q][1]) + (v[q][2] * v[q][2] + v[q][3] * v[q][3]); }
;             const float rstd = 1.0f / sqrtf(wave_sum(qq) * (1.0f / DM) + LN_EPS);
; #pragma unroll
;             for (int q = 0; q < 4; ++q) v[q] = v[q] * rstd * lg[q] + lb[q];
;             if (final_out) { if (row >= NCTX) {
; #pragma unroll
;                 for (int q = 0; q < 4; ++q) *(f32x4*)(F.out + (size_t)(row - NCTX) * DM + RP_COL(q)) = v[q]; } }
;             else {
; #pragma unroll
;                 for (int j = 0; j < 2; ++j) { u32x4 w; w.x = pk2(v[2 * j][0], v[2 * j][1]); w.y = pk2(v[2 * j][2], v[2 * j][3]); w.z = pk2(v[2 * j + 1][0], v[2 * j + 1][1]); w.w = pk2(v[2 * j + 1][2], v[2 * j + 1][3]);
;                     *(u32x4*)(X + (size_t)row * DM + lc + 512 * j) = w; } }
	ds_swizzle_b32 v98, v0 offset:swizzle(SWAP,16)
	s_waitcnt lgkmcnt(0)
	v_add_f32_e32 v0, v0, v98
	v_mov_b32_e32 v98, v0
	s_nop 1
	v_permlane32_swap_b32_e32 v0, v98
	v_add_f32_e32 v0, v0, v98
	v_fmac_f32_e32 v91, 0xba800000, v0
	v_fmac_f32_e32 v93, 0xba800000, v0
	v_fmamk_f32 v90, v0, 0xba800000, v90
	v_fmamk_f32 v92, v0, 0xba800000, v92
	v_mul_f32_e32 v98, v93, v93
	v_mul_f32_e32 v99, v91, v91
	v_fmac_f32_e32 v98, v92, v92
	v_fmac_f32_e32 v99, v90, v90
	v_fmac_f32_e32 v95, 0xba800000, v0
	v_fmac_f32_e32 v141, 0xba800000, v0
	v_add_f32_e32 v98, v98, v99
	v_fmamk_f32 v94, v0, 0xba800000, v94
	v_fmamk_f32 v140, v0, 0xba800000, v140
	v_mul_f32_e32 v99, v141, v141
	v_mul_f32_e32 v100, v95, v95
	v_fmac_f32_e32 v99, v140, v140
	v_fmac_f32_e32 v100, v94, v94
	v_add_f32_e32 v99, v99, v100
	v_fmac_f32_e32 v145, 0xba800000, v0
	v_fmac_f32_e32 v143, 0xba800000, v0
	v_add_f32_e32 v98, v98, v99
	v_fmamk_f32 v144, v0, 0xba800000, v144
	v_fmamk_f32 v142, v0, 0xba800000, v142
	v_mul_f32_e32 v99, v143, v143
	v_mul_f32_e32 v100, v145, v145
	v_fmac_f32_e32 v99, v142, v142
	v_fmac_f32_e32 v100, v144, v144
	v_add_f32_e32 v99, v99, v100
	v_fmac_f32_e32 v149, 0xba800000, v0
	v_fmac_f32_e32 v97, 0xba800000, v0
	v_add_f32_e32 v98, v99, v98
	v_fmamk_f32 v148, v0, 0xba800000, v148
	v_fmamk_f32 v96, v0, 0xba800000, v96
	v_mul_f32_e32 v0, v97, v97
	v_mul_f32_e32 v99, v149, v149
	v_fmac_f32_e32 v0, v96, v96
	v_fmac_f32_e32 v99, v148, v148
	v_add_f32_e32 v0, v0, v99
	v_add_f32_e32 v0, v0, v98
	s_nop 1
	v_add_f32_dpp v0, v0, v0 quad_perm:[1,0,3,2] row_mask:0xf bank_mask:0xf
	s_nop 1
	v_add_f32_dpp v0, v0, v0 quad_perm:[2,3,0,1] row_mask:0xf bank_mask:0xf
	s_nop 1
	v_add_f32_dpp v0, v0, v0 row_half_mirror row_mask:0xf bank_mask:0xf
	s_nop 1
	v_add_f32_dpp v0, v0, v0 row_mirror row_mask:0xf bank_mask:0xf
	s_waitcnt lgkmcnt(0)
	ds_swizzle_b32 v98, v0 offset:swizzle(SWAP,16)
	s_waitcnt lgkmcnt(0)
	v_add_f32_e32 v0, v0, v98
	v_mov_b32_e32 v98, v0
	s_nop 1
	v_permlane32_swap_b32_e32 v0, v98
	v_add_f32_e32 v0, v0, v98
	v_fmamk_f32 v0, v0, 0x3a800000, v188
	v_cmp_gt_f32_e32 vcc, s31, v0
	v_mul_f32_e32 v98, 0x4f800000, v0
	s_nop 0
	v_cndmask_b32_e32 v0, v0, v98, vcc
	v_sqrt_f32_e32 v98, v0
	s_nop 0
	v_add_u32_e32 v99, -1, v98
	v_fma_f32 v100, -v99, v98, v0
	v_cmp_ge_f32_e64 s[4:5], 0, v100
	v_add_u32_e32 v100, 1, v98
	s_nop 0
	v_cndmask_b32_e64 v99, v98, v99, s[4:5]
	v_fma_f32 v98, -v100, v98, v0
	v_cmp_lt_f32_e64 s[4:5], 0, v98
	s_nop 1
	v_cndmask_b32_e64 v98, v99, v100, s[4:5]
	v_mul_f32_e32 v99, 0x37800000, v98
	v_cndmask_b32_e32 v98, v98, v99, vcc
	v_cmp_class_f32_e32 vcc, v0, v189
	s_nop 1
	v_cndmask_b32_e32 v0, v98, v0, vcc
	v_div_scale_f32 v98, s[0:1], v0, v0, 1.0
	v_rcp_f32_e32 v99, v98
	s_mov_b64 s[0:1], -1
	v_fma_f32 v100, -v98, v99, 1.0
	v_fmac_f32_e32 v99, v100, v99
	v_div_scale_f32 v100, vcc, 1.0, v0, 1.0
	v_mul_f32_e32 v101, v100, v99
	v_fma_f32 v102, -v98, v101, v100
	v_fmac_f32_e32 v101, v102, v99
	v_fma_f32 v98, -v98, v101, v100
	v_div_fmas_f32 v98, v98, v99, v101
	v_div_fixup_f32 v0, v98, v0, 1.0
	v_pk_mul_f32 v[92:93], v[92:93], v[0:1] op_sel_hi:[1,0]
	v_pk_mul_f32 v[90:91], v[90:91], v[0:1] op_sel_hi:[1,0]
	v_pk_fma_f32 v[98:99], v[2:3], v[92:93], v[6:7]
	v_pk_fma_f32 v[100:101], v[4:5], v[90:91], v[8:9]
	v_pk_mul_f32 v[90:91], v[140:141], v[0:1] op_sel_hi:[1,0]
	v_pk_mul_f32 v[92:93], v[94:95], v[0:1] op_sel_hi:[1,0]
	v_pk_fma_f32 v[102:103], v[10:11], v[90:91], v[14:15]
	v_pk_fma_f32 v[104:105], v[12:13], v[92:93], v[16:17]
	v_pk_mul_f32 v[90:91], v[142:143], v[0:1] op_sel_hi:[1,0]
	v_pk_mul_f32 v[92:93], v[144:145], v[0:1] op_sel_hi:[1,0]
	v_pk_mul_f32 v[94:95], v[96:97], v[0:1] op_sel_hi:[1,0]
	v_pk_mul_f32 v[96:97], v[148:149], v[0:1] op_sel_hi:[1,0]
	v_pk_fma_f32 v[92:93], v[20:21], v[92:93], v[24:25]
	v_pk_fma_f32 v[90:91], v[18:19], v[90:91], v[22:23]
	v_pk_fma_f32 v[96:97], v[28:29], v[96:97], v[32:33]
	v_pk_fma_f32 v[94:95], v[26:27], v[94:95], v[30:31]
	s_waitcnt vmcnt(0)
	s_and_b64 vcc, exec, s[2:3]
	s_cbranch_vccnz .LBB0_1212
	v_bfe_u32 v0, v98, 16, 1
	v_add3_u32 v0, v98, v0, s43
	v_bfe_u32 v107, v99, 16, 1
	v_lshrrev_b32_e32 v0, 16, v0
	v_add3_u32 v107, v99, v107, s43
	v_and_or_b32 v140, v107, s33, v0
	v_bfe_u32 v0, v100, 16, 1
	v_add3_u32 v0, v100, v0, s43
	v_bfe_u32 v107, v101, 16, 1
	v_lshrrev_b32_e32 v0, 16, v0
	v_add3_u32 v107, v101, v107, s43
	v_and_or_b32 v141, v107, s33, v0
	v_bfe_u32 v0, v102, 16, 1
	v_add3_u32 v0, v102, v0, s43
	v_bfe_u32 v107, v103, 16, 1
	v_lshrrev_b32_e32 v0, 16, v0
	v_add3_u32 v107, v103, v107, s43
	v_and_or_b32 v142, v107, s33, v0
	v_bfe_u32 v0, v104, 16, 1
	v_add3_u32 v0, v104, v0, s43
	v_bfe_u32 v107, v105, 16, 1
	v_lshrrev_b32_e32 v0, 16, v0
	v_add3_u32 v107, v105, v107, s43
	v_and_or_b32 v143, v107, s33, v0
	v_bfe_u32 v0, v90, 16, 1
	v_add_co_u32_e32 v144, vcc, s39, v138
	v_add3_u32 v0, v90, v0, s43
	v_bfe_u32 v107, v91, 16, 1
	v_addc_co_u32_e32 v145, vcc, 0, v139, vcc
	v_lshrrev_b32_e32 v0, 16, v0
	v_add3_u32 v107, v91, v107, s43
	global_store_dwordx4 v[144:145], v[140:143], off
	s_mov_b64 s[0:1], 0
	s_nop 0
	v_and_or_b32 v140, v107, s33, v0
	v_bfe_u32 v0, v92, 16, 1
	v_add3_u32 v0, v92, v0, s43
	v_bfe_u32 v107, v93, 16, 1
	v_lshrrev_b32_e32 v0, 16, v0
	v_add3_u32 v107, v93, v107, s43
	v_and_or_b32 v141, v107, s33, v0
	v_bfe_u32 v0, v94, 16, 1
	v_add3_u32 v0, v94, v0, s43
	v_bfe_u32 v107, v95, 16, 1
	v_lshrrev_b32_e32 v0, 16, v0
	v_add3_u32 v107, v95, v107, s43
	v_and_or_b32 v142, v107, s33, v0
	v_bfe_u32 v0, v96, 16, 1
	v_add3_u32 v0, v96, v0, s43
	v_bfe_u32 v107, v97, 16, 1
	v_lshrrev_b32_e32 v0, 16, v0
	v_add3_u32 v107, v97, v107, s43
	v_and_or_b32 v143, v107, s33, v0
	global_store_dwordx4 v[144:145], v[140:143], off offset:1024

; template <int M> __device__ __forceinline__ float swz_xor_f(float v) { return __builtin_bit_cast(float, __builtin_amdgcn_ds_swizzle(__builtin_bit_cast(int, v), (M << 10) | 0x1f)); }
; #define INP(k) inp_ptr(k)
; __device__ __forceinline__ float half_sum32(float v) { v += swz_xor_f<1>(v); v += swz_xor_f<2>(v); v += swz_xor_f<4>(v); v += swz_xor_f<8>(v); v += swz_xor_f<16>(v); return v; }
; __device__ __forceinline__ float wave_sum(float v) {
;     v = half_sum32(v);
;     const auto rr = __builtin_amdgcn_permlane32_swap(__float_as_uint(v), __float_as_uint(v), false, false);
;     return __uint_as_float(rr[0]) + __uint_as_float(rr[1]);
; }
; __device__ __forceinline__ void attn_phase(Frame& F) {
;     const bf16_t* Q = (const bf16_t*)(F.ws + WS_R1 + R1_Q); const bf16_t* Kb = (const bf16_t*)(F.ws + WS_R1 + R1_K); const bf16_t* Vb = (const bf16_t*)(F.ws + WS_R1 + R1_V);
;     bf16_t* O = (bf16_t*)(F.ws + WS_R1 + R1_O); const unsigned char* V8 = F.ws + WS_R1 + R1_V8;
;     float lam;
;     { const float* lp = INP(IN_DLAM); const float a = wave_sum(lp[F.lane] * lp[64 + F.lane]), b = wave_sum(lp[128 + F.lane] * lp[192 + F.lane]); lam = expf(a) - expf(b) + LAM_INIT; }
.LBB0_1286:
	s_nop 0
	s_nop 0
	s_nop 0
	s_nop 0
	s_nop 0
	s_nop 0
	s_nop 0
	s_nop 0
	s_nop 0
	s_nop 0
	s_nop 0
	s_nop 0
	s_nop 0
	s_nop 0
	s_or_b64 exec, exec, s[2:3]
	s_mov_b32 s0, s53
	s_waitcnt lgkmcnt(0)
	s_barrier
	s_mov_b32 s8, s90
	s_mov_b32 s9, s73
	s_mov_b64 s[74:75], s[94:95]
	s_mov_b64 s[0:1], s[88:89]
	v_mbcnt_lo_u32_b32 v0, -1, 0
	v_mbcnt_hi_u32_b32 v0, -1, v0
	s_load_dwordx2 s[0:1], s[0:1], 0x78
	v_and_b32_e32 v0, 63, v0
	v_lshlrev_b32_e32 v3, 2, v0
	s_waitcnt lgkmcnt(0)
	global_load_dword v0, v3, s[0:1]
	global_load_dword v2, v3, s[0:1] offset:256
	s_waitcnt vmcnt(0)
	v_mul_f32_e32 v4, v0, v2
	ds_swizzle_b32 v4, v4 offset:swizzle(SWAP,1)
	s_waitcnt lgkmcnt(0)
	v_fmac_f32_e32 v4, v0, v2
	ds_swizzle_b32 v0, v4 offset:swizzle(SWAP,2)
	s_waitcnt lgkmcnt(0)
	v_add_f32_e32 v0, v4, v0
	global_load_dword v4, v3, s[0:1] offset:512
	s_nop 0
	global_load_dword v3, v3, s[0:1] offset:768
	ds_swizzle_b32 v2, v0 offset:swizzle(SWAP,4)
	s_mov_b64 s[0:1], s[88:89]
	s_load_dwordx2 s[4:5], s[0:1], 0x80
	s_and_b32 s0, s8, 7
	s_waitcnt lgkmcnt(0)
	v_add_f32_e32 v0, v0, v2
	ds_swizzle_b32 v2, v0 offset:swizzle(SWAP,8)
	s_cmp_lg_u32 s0, 0
	s_waitcnt lgkmcnt(0)
	v_add_f32_e32 v0, v0, v2
	ds_swizzle_b32 v2, v0 offset:swizzle(SWAP,16)
	s_waitcnt lgkmcnt(0)
	v_add_f32_e32 v0, v0, v2
	v_mov_b32_e32 v2, v0
	s_nop 1
	v_permlane32_swap_b32_e32 v0, v2
	s_waitcnt vmcnt(0)
	v_mul_f32_e32 v5, v4, v3
	ds_swizzle_b32 v5, v5 offset:swizzle(SWAP,1)
	s_waitcnt lgkmcnt(0)
	v_fmac_f32_e32 v5, v4, v3
	ds_swizzle_b32 v3, v5 offset:swizzle(SWAP,2)
	s_waitcnt lgkmcnt(0)
	v_add_f32_e32 v3, v5, v3
	ds_swizzle_b32 v4, v3 offset:swizzle(SWAP,4)
	s_waitcnt lgkmcnt(0)
	v_add_f32_e32 v3, v3, v4
	ds_swizzle_b32 v4, v3 offset:swizzle(SWAP,8)
	s_waitcnt lgkmcnt(0)
	v_add_f32_e32 v3, v3, v4
	ds_swizzle_b32 v4, v3 offset:swizzle(SWAP,16)
	s_waitcnt lgkmcnt(0)
	v_add_f32_e32 v3, v3, v4
	v_mov_b32_e32 v4, v3
	s_nop 1
	v_permlane32_swap_b32_e32 v3, v4
	s_cbranch_scc0 .LBB0_1288
	s_cmpk_gt_i32 s9, 0xfff
	s_cbranch_scc0 .LBB0_1289
	s_branch .LBB0_1362
